# MoE down-proj stream: last clamped tile requests fetch the next work item's first tiles; next item skips prologue loads
# speedup vs baseline: 1.0622x; 1.0208x over previous
; #define GAS __attribute__((address_space(1)))
; #define LAS __attribute__((address_space(3)))
;     ...
;     const size_t o_hid = out_off ? out_off : WS_HID, o_yr = out_off ? out_off : WS_YR;
;     constexpr int KD = (MODE == 0) ? D : DEXP, NT = KD / 64, NSLAB = (MODE == 0) ? 8 : 16, LDW = (MODE == 0) ? DEXP : D, LDX = KD;
;     const int half = wave & 1, nb16 = lane & 15, kb = 4 * (wave >> 1) + (lane >> 4);
;     const int tk = lane & 15, q = lane >> 4;
;     const GAS char* wmat = (const GAS char*)((MODE == 0) ? (half ? a.inp(I_WEU) : a.inp(I_WEG)) : a.inp(I_WED));
;     const unsigned wvo = (unsigned)((4 * kb * LDW + 4 * nb16) * 4);
;     const int lw0 = (64 * half + 4 * nb16) * 128 + (((kb >> 1) ^ ((2 * nb16) & 7)) << 4) + (kb & 1) * 8, lw1 = lw0 ^ 16;
;     const int rd_g = (tk >> 1) & 7;
;     for (int vb = bid; vb < NEXP * NSLAB; vb += G) {
;         const int xcd = vb & 7, idx = vb >> 3; const int e = xcd * 8 + idx / NSLAB, slab = idx % NSLAB;
;         const int M = __builtin_amdgcn_readfirstlane(lc[LC_CNT / 4 + e]), row0 = __builtin_amdgcn_readfirstlane(lc[LC_PSTART / 4 + e]);
;         const size_t wuo = (MODE == 0) ? ((size_t)(l * NEXP + e) * D * DEXP + slab * 64) * 4 : ((size_t)(l * NEXP + e) * DEXP * D + slab * 128 + 64 * half) * 4;
;         const __amdgpu_buffer_rsrc_t wrs = __builtin_amdgcn_make_buffer_rsrc((void*)(wmat + wuo), 0, KD * LDW * 4, 0x00020000);
;         const __amdgpu_buffer_rsrc_t xrs = __builtin_amdgcn_make_buffer_rsrc((MODE == 0) ? (void*)(ws + WS_U) : (void*)((const GAS char*)(ws + WS_HID) + (size_t)row0 * LDX * 2), 0, 0x7fffffff, 0x00020000);
;         const int* el = (const int*)(ws + WS_ELIST) + (size_t)e * T;
;         for (int rp = 0; rp < M; rp += 384) {
;             unsigned xso[6];
; #pragma unroll
;             for (int i = 0; i < 6; ++i) { int tok = rp + wave * 48 + 8 * i + (lane >> 3); tok = min(tok, M - 1); if (VAR == 5) tok &= 15; if (MODE == 0) tok = el[tok]; xso[i] = (unsigned)(tok * LDX * 2 + (lane & 7) * 16); }
;             LAS unsigned char* xw = lds + MS_XOFF + wave * MS_XWAVE; const int xwo = (lane >> 3) * 128 + (((lane & 7) ^ ((lane >> 4) & 3)) << 4);
;             const LAS unsigned char* xr = lds + MS_XOFF + wave * MS_XWAVE + tk * 128 + ((q ^ rd_g) << 4);
.LBB0_1778:
	s_mov_b32 s83, 0
	s_mov_b32 s10, 0x7ffffff0
	s_waitcnt vmcnt(7)
	v_mov_b32_e32 v2, v0
	s_load_dwordx4 s[0:3], s[74:75], 0x108
	s_mov_b64 s[4:5], s[74:75]
	s_waitcnt lgkmcnt(0)
	s_load_dword s0, s[78:79], 0x0
	s_mov_b32 s1, s72
	s_waitcnt lgkmcnt(0)
	s_cmpk_gt_i32 s1, 0x3ff
	v_readfirstlane_b32 s7, v2
	s_cbranch_scc1 .LBB0_1792
	s_ashr_i32 s8, s7, 6
	s_load_dwordx2 s[12:13], s[4:5], 0xf8
	v_and_b32_e32 v3, 15, v2
	s_lshl_b32 s4, s8, 1
	v_bfe_u32 v4, v2, 4, 2
	v_and_or_b32 v5, s4, -4, v4
	s_waitcnt vmcnt(0)
	v_lshlrev_b32_e32 v6, 4, v3
	s_and_b32 s94, s7, 64
	v_lshlrev_b32_e32 v90, 3, v4
	v_lshl_or_b32 v160, v5, 15, v6
	v_lshlrev_b32_e32 v6, 9, v3
	s_lshl_b32 s4, s94, 7
	v_and_b32_e32 v7, 8, v90
	v_or3_b32 v6, s4, v6, v7
	v_readlane_b32 s4, v255, 30
	s_lshl_b32 s26, s4, 6
	s_mul_i32 s4, s8, 16
	s_mul_i32 s80, s8, 16
	v_bfe_u32 v8, v2, 3, 3
	v_lshrrev_b32_e32 v5, 1, v5
	v_lshlrev_b32_e32 v7, 1, v2
	v_or_b32_e32 v162, s4, v8
	v_lshlrev_b32_e32 v8, 4, v2
	v_bitop3_b32 v5, v5, v7, 6 bitop3:0x78
	v_and_b32_e32 v163, 0x70, v8
	v_bitop3_b32 v8, v4, v2, 7 bitop3:0x78
	v_lshl_add_u32 v161, v5, 4, v6
	v_lshrrev_b32_e32 v6, 1, v2
	v_bfe_u32 v7, v2, 1, 3
	s_add_u32 s27, s2, 0x2fe31000
	s_mulk_i32 s8, 0x3000
	v_and_or_b32 v2, v2, 56, v8
	s_addc_u32 s28, s3, 0
	s_add_i32 s29, s8, 0
	v_lshlrev_b32_e32 v172, 4, v2
	v_lshlrev_b32_e32 v2, 7, v3
	v_add_u32_e32 v173, s29, v2
	v_add_u32_e32 v176, 0, v2
	v_or_b32_e32 v177, s4, v3
	v_lshl_add_u64 v[2:3], s[2:3], 0, v[90:91]
	s_mov_b64 s[2:3], 0x31e31000
	v_xor_b32_e32 v5, 16, v161
	v_bitop3_b32 v6, v6, v4, 7 bitop3:0x6c
	v_bitop3_b32 v4, v4, v7, 4 bitop3:0x36
	v_lshl_add_u64 v[156:157], v[2:3], 0, s[2:3]
	v_xor_b32_e32 v2, 64, v172
	v_lshlrev_b32_e32 v174, 4, v6
	v_lshlrev_b32_e32 v175, 4, v4
	v_or_b32_e32 v90, 0x2000, v160
	v_or_b32_e32 v178, 0x4000, v160
	v_or_b32_e32 v179, 0x6000, v160
	v_add_u32_e32 v180, 0, v5
	v_add_u32_e32 v181, s29, v2
	v_readlane_b32 s5, v255, 31
	s_branch .LBB0_1781

; #define GAS __attribute__((address_space(1)))
; #define LAS __attribute__((address_space(3)))
; #define MS_WLOAD(set, t) do { _Pragma("unroll") for (int r_ = 0; r_ < 4; ++r_) wr[set][r_] = __builtin_bit_cast(f32x4, __builtin_amdgcn_raw_buffer_load_b128(wrs, (int)wvo + r_ * LDW * 4, MS_CL(t) * (64 * LDW * 4), 0)); } while (0)
;     ...
;     for (int vb = bid; vb < NEXP * NSLAB; vb += G) {
;         const int xcd = vb & 7, idx = vb >> 3; const int e = xcd * 8 + idx / NSLAB, slab = idx % NSLAB;
;         const int M = __builtin_amdgcn_readfirstlane(lc[LC_CNT / 4 + e]), row0 = __builtin_amdgcn_readfirstlane(lc[LC_PSTART / 4 + e]);
;         const size_t wuo = (MODE == 0) ? ((size_t)(l * NEXP + e) * D * DEXP + slab * 64) * 4 : ((size_t)(l * NEXP + e) * DEXP * D + slab * 128 + 64 * half) * 4;
;         const __amdgpu_buffer_rsrc_t wrs = __builtin_amdgcn_make_buffer_rsrc((void*)(wmat + wuo), 0, KD * LDW * 4, 0x00020000);
;         const __amdgpu_buffer_rsrc_t xrs = __builtin_amdgcn_make_buffer_rsrc((MODE == 0) ? (void*)(ws + WS_U) : (void*)((const GAS char*)(ws + WS_HID) + (size_t)row0 * LDX * 2), 0, 0x7fffffff, 0x00020000);
;         const int* el = (const int*)(ws + WS_ELIST) + (size_t)e * T;
;         for (int rp = 0; rp < M; rp += 384) {
;             unsigned xso[6];
; #pragma unroll
;             for (int i = 0; i < 6; ++i) { int tok = rp + wave * 48 + 8 * i + (lane >> 3); tok = min(tok, M - 1); if (VAR == 5) tok &= 15; if (MODE == 0) tok = el[tok]; xso[i] = (unsigned)(tok * LDX * 2 + (lane & 7) * 16); }
;             LAS unsigned char* xw = lds + MS_XOFF + wave * MS_XWAVE; const int xwo = (lane >> 3) * 128 + (((lane & 7) ^ ((lane >> 4) & 3)) << 4);
;             const LAS unsigned char* xr = lds + MS_XOFF + wave * MS_XWAVE + tk * 128 + ((q ^ rd_g) << 4);
;             f32x4 acc[3][8];
; #pragma unroll
;             for (int mt = 0; mt < 3; ++mt)
; #pragma unroll
;                 for (int j = 0; j < 8; ++j) acc[mt][j] = (f32x4){0.f, 0.f, 0.f, 0.f};
;             f32x4 wr[2][4];
;             bf16x8 xs[6];
;     ...
;             const LAS unsigned char* xr1 = lds + MS_XOFF + wave * MS_XWAVE + tk * 128 + (((4 + q) ^ rd_g) << 4);
;             __syncthreads();
;             MS_XSLOAD(0); MS_WLOAD(0, 0); MS_WLOAD(1, 1);
;             MS_WCOMMIT(0, 0); MS_WLOAD(0, 2);
;             MS_XSWRITE(0); MS_XSLOAD(1);
;             __syncthreads();
.LBB0_1781:
	s_ashr_i32 s2, s1, 3
	s_lshr_b32 s4, s2, 28
	s_lshl_b32 s3, s1, 3
	s_add_i32 s4, s2, s4
	s_and_b32 s3, s3, 56
	s_ashr_i32 s4, s4, 4
	s_add_i32 s3, s3, s4
	s_lshl_b32 s5, s3, 2
	s_add_i32 s5, s5, 0
	s_add_i32 s5, s5, 0x20000
	v_mov_b32_e32 v240, s5
	v_mov_b32_e32 v242, s5
	ds_read2_b32 v[240:241], v240 offset0:136 offset1:200
	ds_read2_b32 v[242:243], v242 offset0:138 offset1:202
	s_add_i32 s91, s1, 0x100
	s_waitcnt lgkmcnt(0)
	v_readfirstlane_b32 s30, v241
	v_readfirstlane_b32 s24, v240
	v_readfirstlane_b32 s89, v243
	v_readfirstlane_b32 s90, v242
	s_cmpk_gt_i32 s91, 0x3ff
	s_cselect_b32 s89, 0, s89
	s_cmpk_lg_i32 s0, 0x100
	s_cselect_b32 s89, 0, s89
	s_cmp_lt_i32 s30, 1
	s_cbranch_scc1 .LBB0_1780
	s_lshl_b32 s4, s4, 4
	s_sub_i32 s4, s2, s4
	s_add_i32 s2, s3, s26
	s_ashr_i32 s3, s2, 31
	s_lshl_b32 s34, s4, 7
	s_lshl_b64 s[2:3], s[2:3], 20
	s_ashr_i32 s35, s34, 31
	s_add_u32 s2, s2, s34
	s_addc_u32 s3, s3, s35
	s_or_b64 s[2:3], s[2:3], s[94:95]
	s_lshl_b64 s[2:3], s[2:3], 2
	s_add_u32 s8, s12, s2
	s_addc_u32 s2, s13, s3
	s_ashr_i32 s25, s24, 31
	s_and_b32 s9, s2, 0xffff
	s_lshl_b64 s[2:3], s[24:25], 10
	s_add_u32 s4, s27, s2
	s_addc_u32 s2, s28, s3
	s_and_b32 s5, s2, 0xffff
	s_mov_b32 s7, s11
	s_add_i32 s25, s30, -1
	v_lshl_add_u64 v[158:159], s[34:35], 1, v[156:157]
	s_mov_b32 s31, 0
	s_branch .LBB0_1784
.LBB0_1783:
	s_or_b64 exec, exec, s[2:3]
	s_mov_b32 s83, s84
	s_addk_i32 s31, 0x180
	s_cmp_ge_i32 s31, s30
	s_cbranch_scc1 .LBB0_1780
.LBB0_1784:
	s_add_i32 s87, s31, 0x180
	s_cmp_lt_i32 s87, s30
	s_cbranch_scc1 .Lxl_same
	s_cmp_lt_i32 s89, 1
	s_cbranch_scc1 .Lxl_none
	s_mov_b32 s84, 1
	s_add_i32 s86, s89, -1
	s_mov_b32 s87, 0
	s_sub_i32 s88, s90, s24
	s_mov_b32 s85, 0x800000
	s_branch .Lxl_sel
.Lxl_same:
	s_mov_b32 s84, 1
	s_mov_b32 s86, s25
	s_mov_b32 s88, 0
	s_mov_b32 s85, 0
	s_branch .Lxl_sel
.Lxl_none:
	s_mov_b32 s84, 0
	s_mov_b32 s85, 0x280000
.Lxl_sel:
	v_add_u32_e32 v240, s31, v162
	v_min_i32_e32 v241, s25, v240
	v_lshl_or_b32 v182, v241, 10, v163
	v_or_b32_e32 v241, 8, v240
	v_min_i32_e32 v241, s25, v241
	v_lshl_or_b32 v183, v241, 10, v163
	v_add_u32_e32 v241, 0x80, v240
	v_min_i32_e32 v241, s25, v241
	v_lshl_or_b32 v184, v241, 10, v163
	v_add_u32_e32 v241, 0x88, v240
	v_min_i32_e32 v241, s25, v241
	v_lshl_or_b32 v185, v241, 10, v163
	v_add_u32_e32 v241, 0x100, v240
	v_min_i32_e32 v241, s25, v241
	v_lshl_or_b32 v186, v241, 10, v163
	v_add_u32_e32 v241, 0x108, v240
	v_min_i32_e32 v241, s25, v241
	v_lshl_or_b32 v187, v241, 10, v163
	s_cmp_eq_u32 s83, 1
	s_cbranch_scc1 .Lxl_fast
	s_barrier
	buffer_load_dwordx4 v[52:55], v160, s[8:11], 0 offen nt
	buffer_load_dwordx4 v[56:59], v90, s[8:11], 0 offen nt
	buffer_load_dwordx4 v[60:63], v178, s[8:11], 0 offen nt
	buffer_load_dwordx4 v[64:67], v179, s[8:11], 0 offen nt
	buffer_load_dwordx4 v[68:71], v182, s[4:7], 0 offen
	buffer_load_dwordx4 v[72:75], v183, s[4:7], 0 offen
	buffer_load_dwordx4 v[76:79], v184, s[4:7], 0 offen
	buffer_load_dwordx4 v[80:83], v185, s[4:7], 0 offen
	buffer_load_dwordx4 v[84:87], v186, s[4:7], 0 offen
	buffer_load_dwordx4 v[96:99], v187, s[4:7], 0 offen
	buffer_load_dwordx4 v[2:5], v160, s[8:11], s23 offen nt
	buffer_load_dwordx4 v[6:9], v178, s[8:11], s23 offen nt
	buffer_load_dwordx4 v[18:21], v160, s[8:11], s93 offen nt
	buffer_load_dwordx4 v[10:13], v90, s[8:11], s23 offen nt
	buffer_load_dwordx4 v[22:25], v90, s[8:11], s93 offen nt
	buffer_load_dwordx4 v[26:29], v178, s[8:11], s93 offen nt
	buffer_load_dwordx4 v[14:17], v179, s[8:11], s23 offen nt
	buffer_load_dwordx4 v[30:33], v179, s[8:11], s93 offen nt
	buffer_load_dwordx4 v[104:107], v182, s[4:7], s92 offen
	buffer_load_dwordx4 v[92:95], v183, s[4:7], s92 offen
	buffer_load_dwordx4 v[112:115], v184, s[4:7], s92 offen
	buffer_load_dwordx4 v[116:119], v185, s[4:7], s92 offen
	buffer_load_dwordx4 v[100:103], v186, s[4:7], s92 offen
	buffer_load_dwordx4 v[108:111], v187, s[4:7], s92 offen
	v_add_u32_e32 v188, 0, v161
	v_mov_b32_e32 v34, 0
	v_add_u32_e32 v189, s29, v172
	s_mov_b32 s2, -2
	v_mov_b32_e32 v35, v34
	v_mov_b32_e32 v36, v34
	v_mov_b32_e32 v37, v34
	v_mov_b32_e32 v38, v34
	v_mov_b32_e32 v39, v34
	v_mov_b32_e32 v40, v34
	v_mov_b32_e32 v41, v34
	v_mov_b32_e32 v42, v34
	v_mov_b32_e32 v43, v34
	v_mov_b32_e32 v44, v34
	v_mov_b32_e32 v45, v34
	v_mov_b32_e32 v46, v34
	v_mov_b32_e32 v47, v34
	v_mov_b32_e32 v48, v34
	v_mov_b32_e32 v49, v34
	v_mov_b32_e32 v50, v34
	v_mov_b32_e32 v51, v34
	v_mov_b32_e32 v120, v34
	v_mov_b32_e32 v121, v34
	v_mov_b32_e32 v122, v34
	v_mov_b32_e32 v123, v34
	v_mov_b32_e32 v124, v34
	v_mov_b32_e32 v125, v34
	v_mov_b32_e32 v126, v34
	v_mov_b32_e32 v127, v34
	v_mov_b32_e32 v128, v34
	v_mov_b32_e32 v129, v34
	v_mov_b32_e32 v130, v34
	v_mov_b32_e32 v131, v34
	v_mov_b32_e32 v132, v34
	v_mov_b32_e32 v133, v34
	v_mov_b32_e32 v134, v34
	v_mov_b32_e32 v135, v34
	v_mov_b32_e32 v136, v34
	v_mov_b32_e32 v137, v34
	v_mov_b32_e32 v138, v34
	v_mov_b32_e32 v139, v34
	v_mov_b32_e32 v140, v34
	v_mov_b32_e32 v141, v34
	v_mov_b32_e32 v142, v34
	v_mov_b32_e32 v143, v34
	v_mov_b32_e32 v144, v34
	v_mov_b32_e32 v145, v34
	v_mov_b32_e32 v146, v34
	v_mov_b32_e32 v147, v34
	v_mov_b32_e32 v148, v34
	v_mov_b32_e32 v149, v34
	v_mov_b32_e32 v150, v34
	v_mov_b32_e32 v151, v34
	v_mov_b32_e32 v152, v34
	v_mov_b32_e32 v153, v34
	v_mov_b32_e32 v154, v34
	v_mov_b32_e32 v155, v34
	s_waitcnt vmcnt(22)
	v_cvt_pk_bf16_f32 v88, v52, v56
	v_cvt_pk_bf16_f32 v52, v53, v57
	s_waitcnt vmcnt(20)
	v_cvt_pk_bf16_f32 v89, v60, v64
	v_cvt_pk_bf16_f32 v53, v61, v65
	v_cvt_pk_bf16_f32 v56, v54, v58
	v_cvt_pk_bf16_f32 v57, v62, v66
	v_cvt_pk_bf16_f32 v54, v55, v59
	v_cvt_pk_bf16_f32 v55, v63, v67
	ds_write2_b64 v188, v[88:89], v[52:53] offset1:16
	ds_write2_b64 v180, v[56:57], v[54:55] offset0:32 offset1:48
	s_waitcnt vmcnt(19)
; #define LAS __attribute__((address_space(3)))
; #define MS_WLOAD(set, t) do { _Pragma("unroll") for (int r_ = 0; r_ < 4; ++r_) wr[set][r_] = __builtin_bit_cast(f32x4, __builtin_amdgcn_raw_buffer_load_b128(wrs, (int)wvo + r_ * LDW * 4, MS_CL(t) * (64 * LDW * 4), 0)); } while (0)
; #define MS_WCOMMIT(set, bufi) do { LAS unsigned char* wb_ = lds + (bufi) * MS_TILE; _Pragma("unroll") for (int i_ = 0; i_ < 4; ++i_) { \
;             u32x2 p_; p_.x = pk2(wr[set][0][i_], wr[set][1][i_]); p_.y = pk2(wr[set][2][i_], wr[set][3][i_]); \
;             *(LAS u32x2*)(wb_ + ((i_ < 2) ? lw0 : lw1) + i_ * 128) = p_; } } while (0)
; #define MS_XSLOAD(t) do { _Pragma("unroll") for (int i_ = 0; i_ < 6; ++i_) xs[i_] = __builtin_bit_cast(bf16x8, __builtin_amdgcn_raw_buffer_load_b128(xrs, (int)xso[i_], MS_CL(t) * 128, 0)); } while (0)
; #define MS_XSWRITE(bufi) do { _Pragma("unroll") for (int i_ = 0; i_ < 6; ++i_) *(LAS bf16x8*)(xw + (bufi) * MS_XBUF + i_ * 1024 + ((i_ & 1) ? (xwo ^ 64) : xwo)) = xs[i_]; } while (0)
; #define MS_STEP(I, J, t) do { MS_WCOMMIT(J, J); MS_WLOAD(J, (t) + 3); MS_COMPUTE(I); MS_XSWRITE(J); MS_XSLOAD((t) + 2); __syncthreads(); } while (0)
;     ...
;             f32x4 acc[3][8];
; #pragma unroll
;             for (int mt = 0; mt < 3; ++mt)
; #pragma unroll
;                 for (int j = 0; j < 8; ++j) acc[mt][j] = (f32x4){0.f, 0.f, 0.f, 0.f};
;             f32x4 wr[2][4];
;             bf16x8 xs[6];
;     ...
;             const LAS unsigned char* xr1 = lds + MS_XOFF + wave * MS_XWAVE + tk * 128 + (((4 + q) ^ rd_g) << 4);
;             __syncthreads();
;             MS_XSLOAD(0); MS_WLOAD(0, 0); MS_WLOAD(1, 1);
;             MS_WCOMMIT(0, 0); MS_WLOAD(0, 2);
;             MS_XSWRITE(0); MS_XSLOAD(1);
;             __syncthreads();
; #pragma unroll 1
;             for (int t = 0; t < NT; t += 2) { MS_STEP(0, 1, t); MS_STEP(1, 0, t + 1); }
	ds_write_b128 v189, v[68:71] offset:32768
	s_waitcnt vmcnt(18)
	ds_write_b128 v181, v[72:75] offset:33792
	s_waitcnt vmcnt(17)
	ds_write_b128 v189, v[76:79] offset:34816
	s_waitcnt vmcnt(16)
	ds_write_b128 v181, v[80:83] offset:35840
	s_waitcnt vmcnt(15)
	ds_write_b128 v189, v[84:87] offset:36864
	s_waitcnt vmcnt(14)
	ds_write_b128 v181, v[96:99] offset:37888
	v_mov_b32_e32 v52, v34
	v_mov_b32_e32 v53, v34
	v_mov_b32_e32 v54, v34
	v_mov_b32_e32 v55, v34
	v_mov_b32_e32 v56, v34
	v_mov_b32_e32 v57, v34
	v_mov_b32_e32 v58, v34
	v_mov_b32_e32 v59, v34
	v_mov_b32_e32 v60, v34
	v_mov_b32_e32 v61, v34
	v_mov_b32_e32 v62, v34
	v_mov_b32_e32 v63, v34
	v_mov_b32_e32 v64, v34
	v_mov_b32_e32 v65, v34
	v_mov_b32_e32 v66, v34
	v_mov_b32_e32 v67, v34
	v_mov_b32_e32 v68, v34
	v_mov_b32_e32 v69, v34
	v_mov_b32_e32 v70, v34
	v_mov_b32_e32 v71, v34
	v_mov_b32_e32 v72, v34
	v_mov_b32_e32 v73, v34
	v_mov_b32_e32 v74, v34
	v_mov_b32_e32 v75, v34
	v_mov_b32_e32 v76, v34
	v_mov_b32_e32 v77, v34
	v_mov_b32_e32 v78, v34
	v_mov_b32_e32 v79, v34
	v_mov_b32_e32 v80, v34
	v_mov_b32_e32 v81, v34
	v_mov_b32_e32 v82, v34
	v_mov_b32_e32 v83, v34
	v_mov_b32_e32 v84, v34
	v_mov_b32_e32 v85, v34
	v_mov_b32_e32 v86, v34
	v_mov_b32_e32 v87, v34
	v_mov_b32_e32 v88, v34
	v_mov_b32_e32 v89, v34
	v_mov_b32_e32 v96, v34
	v_mov_b32_e32 v97, v34
	v_mov_b32_e32 v98, v34
	v_mov_b32_e32 v99, v34
	s_waitcnt lgkmcnt(0)
	s_barrier
.Lxl_disp:
	s_sub_i32 s81, s30, s31
	s_add_i32 s82, s80, 0x100
	s_cmp_gt_i32 s81, s82
	s_cbranch_scc1 .LBB0_1785
	s_cmp_eq_u32 s84, 0
	s_cbranch_scc1 .Lmoe_l_b
	s_add_i32 s81, s86, 1
	s_sub_i32 s81, s81, s87
	s_cmp_le_i32 s81, s82
	s_cbranch_scc1 .Lmoe_l_b
.LBB0_1785:
	s_add_i32 s2, s2, 2
	s_min_u32 s3, s2, 4
	s_lshl_b32 s33, s3, 19
	s_add_i32 s33, s33, 0x180000
	s_add_i32 s40, s85, 0x80000
	s_cmp_gt_u32 s2, 4
	s_cselect_b32 s33, s40, s33
	s_waitcnt vmcnt(10)
	v_cvt_pk_bf16_f32 v164, v2, v10
	s_waitcnt vmcnt(7)
	v_cvt_pk_bf16_f32 v165, v6, v14
	v_cvt_pk_bf16_f32 v166, v3, v11
	v_cvt_pk_bf16_f32 v167, v7, v15
	v_cvt_pk_bf16_f32 v190, v4, v12
	v_cvt_pk_bf16_f32 v191, v8, v16
	v_cvt_pk_bf16_f32 v192, v5, v13
	v_cvt_pk_bf16_f32 v193, v9, v17
	buffer_load_dwordx4 v[2:5], v160, s[8:11], s33 offen nt
	buffer_load_dwordx4 v[10:13], v90, s[8:11], s33 offen nt
	buffer_load_dwordx4 v[6:9], v178, s[8:11], s33 offen nt
	buffer_load_dwordx4 v[14:17], v179, s[8:11], s33 offen nt
	v_add_u32_e32 v194, 0x4000, v188
	v_add_u32_e32 v195, 0x4000, v180
	v_add_u32_e32 v214, v173, v174
	ds_write2_b64 v194, v[164:165], v[166:167] offset1:16
	ds_write2_b64 v195, v[190:191], v[192:193] offset0:32 offset1:48
	v_add_u32_e32 v215, v176, v174
	ds_read_b128 v[164:167], v214 offset:32768
	ds_read_b128 v[190:193], v214 offset:34816
	ds_read_b128 v[194:197], v214 offset:36864
	ds_read_b128 v[198:201], v215
	ds_read_b128 v[202:205], v215 offset:2048
	ds_read_b128 v[206:209], v215 offset:4096
	ds_read_b128 v[210:213], v215 offset:6144
	s_waitcnt lgkmcnt(3)
	v_mfma_f32_16x16x32_bf16 v[152:155], v[198:201], v[164:167], v[152:155]
	v_mfma_f32_16x16x32_bf16 v[120:123], v[198:201], v[190:193], v[120:123]
	v_mfma_f32_16x16x32_bf16 v[62:65], v[198:201], v[194:197], v[62:65]
	s_waitcnt lgkmcnt(2)
	v_mfma_f32_16x16x32_bf16 v[148:151], v[202:205], v[164:167], v[148:151]
	v_mfma_f32_16x16x32_bf16 v[96:99], v[202:205], v[190:193], v[96:99]
	v_mfma_f32_16x16x32_bf16 v[58:61], v[202:205], v[194:197], v[58:61]
	s_waitcnt lgkmcnt(1)
	v_mfma_f32_16x16x32_bf16 v[144:147], v[206:209], v[164:167], v[144:147]
	v_mfma_f32_16x16x32_bf16 v[86:89], v[206:209], v[190:193], v[86:89]
	v_mfma_f32_16x16x32_bf16 v[54:57], v[206:209], v[194:197], v[54:57]
	s_waitcnt lgkmcnt(0)
	v_mfma_f32_16x16x32_bf16 v[140:143], v[210:213], v[164:167], v[140:143]
	v_mfma_f32_16x16x32_bf16 v[82:85], v[210:213], v[190:193], v[82:85]
	v_mfma_f32_16x16x32_bf16 v[50:53], v[210:213], v[194:197], v[50:53]
	ds_read_b128 v[198:201], v215 offset:8192
	ds_read_b128 v[202:205], v215 offset:10240
	ds_read_b128 v[206:209], v215 offset:12288
	ds_read_b128 v[210:213], v215 offset:14336
	s_waitcnt lgkmcnt(3)
	v_mfma_f32_16x16x32_bf16 v[136:139], v[198:201], v[164:167], v[136:139]
	v_mfma_f32_16x16x32_bf16 v[78:81], v[198:201], v[190:193], v[78:81]
	v_mfma_f32_16x16x32_bf16 v[46:49], v[198:201], v[194:197], v[46:49]
	s_waitcnt lgkmcnt(2)
	v_mfma_f32_16x16x32_bf16 v[132:135], v[202:205], v[164:167], v[132:135]
	v_mfma_f32_16x16x32_bf16 v[74:77], v[202:205], v[190:193], v[74:77]
	v_mfma_f32_16x16x32_bf16 v[42:45], v[202:205], v[194:197], v[42:45]
	s_waitcnt lgkmcnt(1)
	v_mfma_f32_16x16x32_bf16 v[128:131], v[206:209], v[164:167], v[128:131]
	v_mfma_f32_16x16x32_bf16 v[70:73], v[206:209], v[190:193], v[70:73]
	v_mfma_f32_16x16x32_bf16 v[38:41], v[206:209], v[194:197], v[38:41]
	s_waitcnt lgkmcnt(0)
	v_mfma_f32_16x16x32_bf16 v[124:127], v[210:213], v[164:167], v[124:127]
	v_mfma_f32_16x16x32_bf16 v[66:69], v[210:213], v[190:193], v[66:69]
	v_mfma_f32_16x16x32_bf16 v[34:37], v[210:213], v[194:197], v[34:37]
	v_add_u32_e32 v216, v173, v175
	ds_read_b128 v[164:167], v216 offset:32768
	ds_read_b128 v[190:193], v216 offset:34816
	v_add_u32_e32 v217, v176, v175
	ds_read_b128 v[194:197], v216 offset:36864
	ds_read_b128 v[198:201], v217
	ds_read_b128 v[202:205], v217 offset:2048
	ds_read_b128 v[206:209], v217 offset:4096
	ds_read_b128 v[210:213], v217 offset:6144
	s_waitcnt lgkmcnt(3)
	v_mfma_f32_16x16x32_bf16 v[152:155], v[198:201], v[164:167], v[152:155]
	v_mfma_f32_16x16x32_bf16 v[120:123], v[198:201], v[190:193], v[120:123]
	v_mfma_f32_16x16x32_bf16 v[62:65], v[198:201], v[194:197], v[62:65]
	s_waitcnt lgkmcnt(2)
	v_mfma_f32_16x16x32_bf16 v[148:151], v[202:205], v[164:167], v[148:151]
	v_mfma_f32_16x16x32_bf16 v[96:99], v[202:205], v[190:193], v[96:99]
	v_mfma_f32_16x16x32_bf16 v[58:61], v[202:205], v[194:197], v[58:61]
	s_waitcnt lgkmcnt(1)
	v_mfma_f32_16x16x32_bf16 v[144:147], v[206:209], v[164:167], v[144:147]
	v_mfma_f32_16x16x32_bf16 v[86:89], v[206:209], v[190:193], v[86:89]
	v_mfma_f32_16x16x32_bf16 v[54:57], v[206:209], v[194:197], v[54:57]
	s_waitcnt lgkmcnt(0)
	v_mfma_f32_16x16x32_bf16 v[140:143], v[210:213], v[164:167], v[140:143]
	v_mfma_f32_16x16x32_bf16 v[82:85], v[210:213], v[190:193], v[82:85]
	v_mfma_f32_16x16x32_bf16 v[50:53], v[210:213], v[194:197], v[50:53]
	ds_read_b128 v[198:201], v217 offset:8192
	ds_read_b128 v[202:205], v217 offset:10240
	ds_read_b128 v[206:209], v217 offset:12288
	ds_read_b128 v[210:213], v217 offset:14336
	s_min_u32 s33, s2, 5
	s_lshl_b32 s33, s33, 7
	s_waitcnt vmcnt(9)
	ds_write_b128 v189, v[104:107] offset:38912
	s_waitcnt vmcnt(8)
	ds_write_b128 v181, v[92:95] offset:39936
	s_waitcnt vmcnt(7)
	ds_write_b128 v189, v[112:115] offset:40960
	s_waitcnt vmcnt(6)
	ds_write_b128 v181, v[116:119] offset:41984
	s_waitcnt vmcnt(5)
	ds_write_b128 v189, v[100:103] offset:43008
	s_waitcnt vmcnt(4)
	ds_write_b128 v181, v[108:111] offset:44032
	s_addk_i32 s33, 0x100
	s_cmp_lt_u32 s2, 6
	s_cbranch_scc1 .Lxl_nx0
; #define LAS __attribute__((address_space(3)))
; #define MS_WLOAD(set, t) do { _Pragma("unroll") for (int r_ = 0; r_ < 4; ++r_) wr[set][r_] = __builtin_bit_cast(f32x4, __builtin_amdgcn_raw_buffer_load_b128(wrs, (int)wvo + r_ * LDW * 4, MS_CL(t) * (64 * LDW * 4), 0)); } while (0)
; #define MS_WCOMMIT(set, bufi) do { LAS unsigned char* wb_ = lds + (bufi) * MS_TILE; _Pragma("unroll") for (int i_ = 0; i_ < 4; ++i_) { \
;             u32x2 p_; p_.x = pk2(wr[set][0][i_], wr[set][1][i_]); p_.y = pk2(wr[set][2][i_], wr[set][3][i_]); \
;             *(LAS u32x2*)(wb_ + ((i_ < 2) ? lw0 : lw1) + i_ * 128) = p_; } } while (0)
; #define MS_XSLOAD(t) do { _Pragma("unroll") for (int i_ = 0; i_ < 6; ++i_) xs[i_] = __builtin_bit_cast(bf16x8, __builtin_amdgcn_raw_buffer_load_b128(xrs, (int)xso[i_], MS_CL(t) * 128, 0)); } while (0)
; #define MS_XSWRITE(bufi) do { _Pragma("unroll") for (int i_ = 0; i_ < 6; ++i_) *(LAS bf16x8*)(xw + (bufi) * MS_XBUF + i_ * 1024 + ((i_ & 1) ? (xwo ^ 64) : xwo)) = xs[i_]; } while (0)
; #define MS_STEP(I, J, t) do { MS_WCOMMIT(J, J); MS_WLOAD(J, (t) + 3); MS_COMPUTE(I); MS_XSWRITE(J); MS_XSLOAD((t) + 2); __syncthreads(); } while (0)
;     ...
;             const LAS unsigned char* xr1 = lds + MS_XOFF + wave * MS_XWAVE + tk * 128 + (((4 + q) ^ rd_g) << 4);
;             __syncthreads();
;             MS_XSLOAD(0); MS_WLOAD(0, 0); MS_WLOAD(1, 1);
;             MS_WCOMMIT(0, 0); MS_WLOAD(0, 2);
;             MS_XSWRITE(0); MS_XSLOAD(1);
;             __syncthreads();
; #pragma unroll 1
;             for (int t = 0; t < NT; t += 2) { MS_STEP(0, 1, t); MS_STEP(1, 0, t + 1); }
	s_cmp_eq_u32 s84, 0
	s_cbranch_scc1 .Lxl_nx0
	s_mov_b32 s33, 0
	v_add_u32_e32 v240, s87, v162
	v_min_i32_e32 v241, s86, v240
	v_add_u32_e32 v241, s88, v241
	v_lshl_or_b32 v182, v241, 10, v163
	v_or_b32_e32 v241, 8, v240
	v_min_i32_e32 v241, s86, v241
	v_add_u32_e32 v241, s88, v241
	v_lshl_or_b32 v183, v241, 10, v163
	v_add_u32_e32 v241, 0x80, v240
	v_min_i32_e32 v241, s86, v241
	v_add_u32_e32 v241, s88, v241
	v_lshl_or_b32 v184, v241, 10, v163
	v_add_u32_e32 v241, 0x88, v240
	v_min_i32_e32 v241, s86, v241
	v_add_u32_e32 v241, s88, v241
	v_lshl_or_b32 v185, v241, 10, v163
	v_add_u32_e32 v241, 0x100, v240
	v_min_i32_e32 v241, s86, v241
	v_add_u32_e32 v241, s88, v241
	v_lshl_or_b32 v186, v241, 10, v163
	v_add_u32_e32 v241, 0x108, v240
	v_min_i32_e32 v241, s86, v241
	v_add_u32_e32 v241, s88, v241
	v_lshl_or_b32 v187, v241, 10, v163
.Lxl_nx0:
	s_waitcnt lgkmcnt(9)
	v_mfma_f32_16x16x32_bf16 v[136:139], v[198:201], v[164:167], v[136:139]
	buffer_load_dwordx4 v[92:95], v182, s[4:7], s33 offen
	buffer_load_dwordx4 v[100:103], v183, s[4:7], s33 offen
	buffer_load_dwordx4 v[104:107], v184, s[4:7], s33 offen
	buffer_load_dwordx4 v[108:111], v185, s[4:7], s33 offen
	buffer_load_dwordx4 v[112:115], v186, s[4:7], s33 offen
	buffer_load_dwordx4 v[116:119], v187, s[4:7], s33 offen
	s_min_u32 s33, s2, 3
	s_waitcnt lgkmcnt(0)
	v_mfma_f32_16x16x32_bf16 v[132:135], v[202:205], v[164:167], v[132:135]
	s_barrier
	s_lshl_b32 s33, s33, 19
	v_mfma_f32_16x16x32_bf16 v[128:131], v[206:209], v[164:167], v[128:131]
	s_bitset1_b32 s33, 21
	s_sub_i32 s40, s2, 4
	s_lshl_b32 s40, s40, 19
	s_add_i32 s40, s40, s85
	s_cmp_gt_u32 s2, 3
	s_cselect_b32 s33, s40, s33
	v_mfma_f32_16x16x32_bf16 v[124:127], v[210:213], v[164:167], v[124:127]
	v_cvt_pk_bf16_f32 v164, v18, v22
	v_cvt_pk_bf16_f32 v165, v26, v30
	v_cvt_pk_bf16_f32 v18, v19, v23
	v_cvt_pk_bf16_f32 v19, v27, v31
	ds_write2_b64 v188, v[164:165], v[18:19] offset1:16
	v_cvt_pk_bf16_f32 v18, v20, v24
	v_cvt_pk_bf16_f32 v19, v28, v32
	v_cvt_pk_bf16_f32 v20, v21, v25
	v_cvt_pk_bf16_f32 v21, v29, v33
	ds_write2_b64 v180, v[18:19], v[20:21] offset0:32 offset1:48
	buffer_load_dwordx4 v[18:21], v160, s[8:11], s33 offen nt
	buffer_load_dwordx4 v[22:25], v90, s[8:11], s33 offen nt
	buffer_load_dwordx4 v[26:29], v178, s[8:11], s33 offen nt
	buffer_load_dwordx4 v[30:33], v179, s[8:11], s33 offen nt
	v_mfma_f32_16x16x32_bf16 v[78:81], v[198:201], v[190:193], v[78:81]
	v_mfma_f32_16x16x32_bf16 v[46:49], v[198:201], v[194:197], v[46:49]
	v_mfma_f32_16x16x32_bf16 v[74:77], v[202:205], v[190:193], v[74:77]
	v_mfma_f32_16x16x32_bf16 v[42:45], v[202:205], v[194:197], v[42:45]
	v_mfma_f32_16x16x32_bf16 v[70:73], v[206:209], v[190:193], v[70:73]
	v_mfma_f32_16x16x32_bf16 v[38:41], v[206:209], v[194:197], v[38:41]
	v_mfma_f32_16x16x32_bf16 v[66:69], v[210:213], v[190:193], v[66:69]
	v_mfma_f32_16x16x32_bf16 v[34:37], v[210:213], v[194:197], v[34:37]
	ds_read_b128 v[164:167], v214 offset:38912
	ds_read_b128 v[190:193], v214 offset:40960
	ds_read_b128 v[194:197], v214 offset:43008
	ds_read_b128 v[198:201], v215 offset:16384
	ds_read_b128 v[202:205], v215 offset:18432
	ds_read_b128 v[206:209], v215 offset:20480
	ds_read_b128 v[210:213], v215 offset:22528
	s_waitcnt lgkmcnt(3)
	v_mfma_f32_16x16x32_bf16 v[152:155], v[198:201], v[164:167], v[152:155]
	v_mfma_f32_16x16x32_bf16 v[120:123], v[198:201], v[190:193], v[120:123]
	v_mfma_f32_16x16x32_bf16 v[62:65], v[198:201], v[194:197], v[62:65]
	s_waitcnt lgkmcnt(2)
	v_mfma_f32_16x16x32_bf16 v[148:151], v[202:205], v[164:167], v[148:151]
	v_mfma_f32_16x16x32_bf16 v[96:99], v[202:205], v[190:193], v[96:99]
	v_mfma_f32_16x16x32_bf16 v[58:61], v[202:205], v[194:197], v[58:61]
	s_waitcnt lgkmcnt(1)
	v_mfma_f32_16x16x32_bf16 v[144:147], v[206:209], v[164:167], v[144:147]
	v_mfma_f32_16x16x32_bf16 v[86:89], v[206:209], v[190:193], v[86:89]
	v_mfma_f32_16x16x32_bf16 v[54:57], v[206:209], v[194:197], v[54:57]
	s_waitcnt lgkmcnt(0)
	v_mfma_f32_16x16x32_bf16 v[140:143], v[210:213], v[164:167], v[140:143]
	v_mfma_f32_16x16x32_bf16 v[82:85], v[210:213], v[190:193], v[82:85]
	v_mfma_f32_16x16x32_bf16 v[50:53], v[210:213], v[194:197], v[50:53]
	ds_read_b128 v[198:201], v215 offset:24576
	ds_read_b128 v[202:205], v215 offset:26624
	ds_read_b128 v[206:209], v215 offset:28672
	ds_read_b128 v[210:213], v215 offset:30720
	s_waitcnt lgkmcnt(3)
	v_mfma_f32_16x16x32_bf16 v[136:139], v[198:201], v[164:167], v[136:139]
	v_mfma_f32_16x16x32_bf16 v[78:81], v[198:201], v[190:193], v[78:81]
	v_mfma_f32_16x16x32_bf16 v[46:49], v[198:201], v[194:197], v[46:49]
	s_waitcnt lgkmcnt(2)
	v_mfma_f32_16x16x32_bf16 v[132:135], v[202:205], v[164:167], v[132:135]
	v_mfma_f32_16x16x32_bf16 v[74:77], v[202:205], v[190:193], v[74:77]
	v_mfma_f32_16x16x32_bf16 v[42:45], v[202:205], v[194:197], v[42:45]
	s_waitcnt lgkmcnt(1)
	v_mfma_f32_16x16x32_bf16 v[128:131], v[206:209], v[164:167], v[128:131]
	v_mfma_f32_16x16x32_bf16 v[70:73], v[206:209], v[190:193], v[70:73]
	v_mfma_f32_16x16x32_bf16 v[38:41], v[206:209], v[194:197], v[38:41]
	s_waitcnt lgkmcnt(0)
	v_mfma_f32_16x16x32_bf16 v[124:127], v[210:213], v[164:167], v[124:127]
	v_mfma_f32_16x16x32_bf16 v[66:69], v[210:213], v[190:193], v[66:69]
	v_mfma_f32_16x16x32_bf16 v[34:37], v[210:213], v[194:197], v[34:37]
	ds_read_b128 v[164:167], v216 offset:38912
	ds_read_b128 v[190:193], v216 offset:40960
	ds_read_b128 v[194:197], v216 offset:43008
	ds_read_b128 v[198:201], v217 offset:16384
	ds_read_b128 v[202:205], v217 offset:18432
	ds_read_b128 v[206:209], v217 offset:20480
	ds_read_b128 v[210:213], v217 offset:22528
	s_waitcnt lgkmcnt(3)
; #define LAS __attribute__((address_space(3)))
; #define MS_WLOAD(set, t) do { _Pragma("unroll") for (int r_ = 0; r_ < 4; ++r_) wr[set][r_] = __builtin_bit_cast(f32x4, __builtin_amdgcn_raw_buffer_load_b128(wrs, (int)wvo + r_ * LDW * 4, MS_CL(t) * (64 * LDW * 4), 0)); } while (0)
; #define MS_WCOMMIT(set, bufi) do { LAS unsigned char* wb_ = lds + (bufi) * MS_TILE; _Pragma("unroll") for (int i_ = 0; i_ < 4; ++i_) { \
;             u32x2 p_; p_.x = pk2(wr[set][0][i_], wr[set][1][i_]); p_.y = pk2(wr[set][2][i_], wr[set][3][i_]); \
;             *(LAS u32x2*)(wb_ + ((i_ < 2) ? lw0 : lw1) + i_ * 128) = p_; } } while (0)
; #define MS_XSLOAD(t) do { _Pragma("unroll") for (int i_ = 0; i_ < 6; ++i_) xs[i_] = __builtin_bit_cast(bf16x8, __builtin_amdgcn_raw_buffer_load_b128(xrs, (int)xso[i_], MS_CL(t) * 128, 0)); } while (0)
; #define MS_XSWRITE(bufi) do { _Pragma("unroll") for (int i_ = 0; i_ < 6; ++i_) *(LAS bf16x8*)(xw + (bufi) * MS_XBUF + i_ * 1024 + ((i_ & 1) ? (xwo ^ 64) : xwo)) = xs[i_]; } while (0)
; #define MS_STEP(I, J, t) do { MS_WCOMMIT(J, J); MS_WLOAD(J, (t) + 3); MS_COMPUTE(I); MS_XSWRITE(J); MS_XSLOAD((t) + 2); __syncthreads(); } while (0)
;     ...
;             const LAS unsigned char* xr1 = lds + MS_XOFF + wave * MS_XWAVE + tk * 128 + (((4 + q) ^ rd_g) << 4);
;             __syncthreads();
;             MS_XSLOAD(0); MS_WLOAD(0, 0); MS_WLOAD(1, 1);
;             MS_WCOMMIT(0, 0); MS_WLOAD(0, 2);
;             MS_XSWRITE(0); MS_XSLOAD(1);
;             __syncthreads();
; #pragma unroll 1
;             for (int t = 0; t < NT; t += 2) { MS_STEP(0, 1, t); MS_STEP(1, 0, t + 1); }
	v_mfma_f32_16x16x32_bf16 v[152:155], v[198:201], v[164:167], v[152:155]
	v_mfma_f32_16x16x32_bf16 v[120:123], v[198:201], v[190:193], v[120:123]
	v_mfma_f32_16x16x32_bf16 v[62:65], v[198:201], v[194:197], v[62:65]
	s_waitcnt lgkmcnt(2)
	v_mfma_f32_16x16x32_bf16 v[148:151], v[202:205], v[164:167], v[148:151]
	v_mfma_f32_16x16x32_bf16 v[96:99], v[202:205], v[190:193], v[96:99]
	v_mfma_f32_16x16x32_bf16 v[58:61], v[202:205], v[194:197], v[58:61]
	s_waitcnt lgkmcnt(1)
	v_mfma_f32_16x16x32_bf16 v[144:147], v[206:209], v[164:167], v[144:147]
	v_mfma_f32_16x16x32_bf16 v[86:89], v[206:209], v[190:193], v[86:89]
	v_mfma_f32_16x16x32_bf16 v[54:57], v[206:209], v[194:197], v[54:57]
	s_waitcnt lgkmcnt(0)
	v_mfma_f32_16x16x32_bf16 v[140:143], v[210:213], v[164:167], v[140:143]
	v_mfma_f32_16x16x32_bf16 v[82:85], v[210:213], v[190:193], v[82:85]
	v_mfma_f32_16x16x32_bf16 v[50:53], v[210:213], v[194:197], v[50:53]
	ds_read_b128 v[198:201], v217 offset:24576
	ds_read_b128 v[202:205], v217 offset:26624
	ds_read_b128 v[206:209], v217 offset:28672
	ds_read_b128 v[210:213], v217 offset:30720
	s_lshl_b32 s3, s3, 7
	s_waitcnt vmcnt(9)
	ds_write_b128 v189, v[92:95] offset:32768
	s_waitcnt vmcnt(8)
	ds_write_b128 v181, v[100:103] offset:33792
	s_waitcnt vmcnt(7)
	ds_write_b128 v189, v[104:107] offset:34816
	s_waitcnt vmcnt(6)
	ds_write_b128 v181, v[108:111] offset:35840
	s_waitcnt vmcnt(5)
	ds_write_b128 v189, v[112:115] offset:36864
	s_waitcnt vmcnt(4)
	ds_write_b128 v181, v[116:119] offset:37888
	s_addk_i32 s3, 0x180
	s_cmp_eq_u32 s2, 6
	s_cselect_b32 s40, s84, 0
	s_cmp_lg_u32 s40, 0
	s_cselect_b32 s3, 0x80, s3
	buffer_load_dwordx4 v[104:107], v182, s[4:7], s3 offen
	buffer_load_dwordx4 v[92:95], v183, s[4:7], s3 offen
	buffer_load_dwordx4 v[112:115], v184, s[4:7], s3 offen
	buffer_load_dwordx4 v[116:119], v185, s[4:7], s3 offen
	buffer_load_dwordx4 v[100:103], v186, s[4:7], s3 offen
	buffer_load_dwordx4 v[108:111], v187, s[4:7], s3 offen
	s_waitcnt lgkmcnt(9)
	v_mfma_f32_16x16x32_bf16 v[136:139], v[198:201], v[164:167], v[136:139]
	s_cmp_gt_u32 s2, 5
	s_waitcnt lgkmcnt(0)
	s_barrier
	v_mfma_f32_16x16x32_bf16 v[78:81], v[198:201], v[190:193], v[78:81]
	v_mfma_f32_16x16x32_bf16 v[46:49], v[198:201], v[194:197], v[46:49]
	v_mfma_f32_16x16x32_bf16 v[132:135], v[202:205], v[164:167], v[132:135]
	v_mfma_f32_16x16x32_bf16 v[74:77], v[202:205], v[190:193], v[74:77]
	v_mfma_f32_16x16x32_bf16 v[42:45], v[202:205], v[194:197], v[42:45]
	v_mfma_f32_16x16x32_bf16 v[128:131], v[206:209], v[164:167], v[128:131]
	v_mfma_f32_16x16x32_bf16 v[70:73], v[206:209], v[190:193], v[70:73]
	v_mfma_f32_16x16x32_bf16 v[38:41], v[206:209], v[194:197], v[38:41]
	v_mfma_f32_16x16x32_bf16 v[124:127], v[210:213], v[164:167], v[124:127]
	v_mfma_f32_16x16x32_bf16 v[66:69], v[210:213], v[190:193], v[66:69]
	v_mfma_f32_16x16x32_bf16 v[34:37], v[210:213], v[194:197], v[34:37]
	s_cbranch_scc0 .LBB0_1785
	s_branch .Lmoe_l_done
.Lmoe_l_b:
	s_add_i32 s2, s2, 2
	s_min_u32 s3, s2, 4
	s_lshl_b32 s33, s3, 19
	s_add_i32 s33, s33, 0x180000
	s_add_i32 s40, s85, 0x80000
	s_cmp_gt_u32 s2, 4
	s_cselect_b32 s33, s40, s33
	s_waitcnt vmcnt(10)
	v_cvt_pk_bf16_f32 v164, v2, v10
	s_waitcnt vmcnt(7)
	v_cvt_pk_bf16_f32 v165, v6, v14
	v_cvt_pk_bf16_f32 v166, v3, v11
	v_cvt_pk_bf16_f32 v167, v7, v15
	v_cvt_pk_bf16_f32 v190, v4, v12
	v_cvt_pk_bf16_f32 v191, v8, v16
	v_cvt_pk_bf16_f32 v192, v5, v13
	v_cvt_pk_bf16_f32 v193, v9, v17
	buffer_load_dwordx4 v[2:5], v160, s[8:11], s33 offen nt
	buffer_load_dwordx4 v[10:13], v90, s[8:11], s33 offen nt
	buffer_load_dwordx4 v[6:9], v178, s[8:11], s33 offen nt
	buffer_load_dwordx4 v[14:17], v179, s[8:11], s33 offen nt
	v_add_u32_e32 v194, 0x4000, v188
	v_add_u32_e32 v195, 0x4000, v180
	v_add_u32_e32 v214, v173, v174
	ds_write2_b64 v194, v[164:165], v[166:167] offset1:16
	ds_write2_b64 v195, v[190:191], v[192:193] offset0:32 offset1:48
	v_add_u32_e32 v215, v176, v174
	ds_read_b128 v[164:167], v214 offset:32768
	ds_read_b128 v[190:193], v214 offset:34816
	ds_read_b128 v[198:201], v215
	ds_read_b128 v[202:205], v215 offset:2048
	ds_read_b128 v[206:209], v215 offset:4096
	ds_read_b128 v[210:213], v215 offset:6144
	s_waitcnt lgkmcnt(3)
	v_mfma_f32_16x16x32_bf16 v[152:155], v[198:201], v[164:167], v[152:155]
	v_mfma_f32_16x16x32_bf16 v[120:123], v[198:201], v[190:193], v[120:123]
	s_waitcnt lgkmcnt(2)
	v_mfma_f32_16x16x32_bf16 v[148:151], v[202:205], v[164:167], v[148:151]
	v_mfma_f32_16x16x32_bf16 v[96:99], v[202:205], v[190:193], v[96:99]
	s_waitcnt lgkmcnt(1)
	v_mfma_f32_16x16x32_bf16 v[144:147], v[206:209], v[164:167], v[144:147]
	v_mfma_f32_16x16x32_bf16 v[86:89], v[206:209], v[190:193], v[86:89]
	s_waitcnt lgkmcnt(0)
	v_mfma_f32_16x16x32_bf16 v[140:143], v[210:213], v[164:167], v[140:143]
	v_mfma_f32_16x16x32_bf16 v[82:85], v[210:213], v[190:193], v[82:85]
	ds_read_b128 v[198:201], v215 offset:8192
	ds_read_b128 v[202:205], v215 offset:10240
	ds_read_b128 v[206:209], v215 offset:12288
	ds_read_b128 v[210:213], v215 offset:14336
	s_waitcnt lgkmcnt(3)
	v_mfma_f32_16x16x32_bf16 v[136:139], v[198:201], v[164:167], v[136:139]
	v_mfma_f32_16x16x32_bf16 v[78:81], v[198:201], v[190:193], v[78:81]
	s_waitcnt lgkmcnt(2)
	v_mfma_f32_16x16x32_bf16 v[132:135], v[202:205], v[164:167], v[132:135]
	v_mfma_f32_16x16x32_bf16 v[74:77], v[202:205], v[190:193], v[74:77]
	s_waitcnt lgkmcnt(1)
	v_mfma_f32_16x16x32_bf16 v[128:131], v[206:209], v[164:167], v[128:131]
	v_mfma_f32_16x16x32_bf16 v[70:73], v[206:209], v[190:193], v[70:73]
	s_waitcnt lgkmcnt(0)
; #define LAS __attribute__((address_space(3)))
; #define MS_WLOAD(set, t) do { _Pragma("unroll") for (int r_ = 0; r_ < 4; ++r_) wr[set][r_] = __builtin_bit_cast(f32x4, __builtin_amdgcn_raw_buffer_load_b128(wrs, (int)wvo + r_ * LDW * 4, MS_CL(t) * (64 * LDW * 4), 0)); } while (0)
; #define MS_WCOMMIT(set, bufi) do { LAS unsigned char* wb_ = lds + (bufi) * MS_TILE; _Pragma("unroll") for (int i_ = 0; i_ < 4; ++i_) { \
;             u32x2 p_; p_.x = pk2(wr[set][0][i_], wr[set][1][i_]); p_.y = pk2(wr[set][2][i_], wr[set][3][i_]); \
;             *(LAS u32x2*)(wb_ + ((i_ < 2) ? lw0 : lw1) + i_ * 128) = p_; } } while (0)
; #define MS_XSLOAD(t) do { _Pragma("unroll") for (int i_ = 0; i_ < 6; ++i_) xs[i_] = __builtin_bit_cast(bf16x8, __builtin_amdgcn_raw_buffer_load_b128(xrs, (int)xso[i_], MS_CL(t) * 128, 0)); } while (0)
; #define MS_XSWRITE(bufi) do { _Pragma("unroll") for (int i_ = 0; i_ < 6; ++i_) *(LAS bf16x8*)(xw + (bufi) * MS_XBUF + i_ * 1024 + ((i_ & 1) ? (xwo ^ 64) : xwo)) = xs[i_]; } while (0)
; #define MS_STEP(I, J, t) do { MS_WCOMMIT(J, J); MS_WLOAD(J, (t) + 3); MS_COMPUTE(I); MS_XSWRITE(J); MS_XSLOAD((t) + 2); __syncthreads(); } while (0)
;     ...
;             const LAS unsigned char* xr1 = lds + MS_XOFF + wave * MS_XWAVE + tk * 128 + (((4 + q) ^ rd_g) << 4);
;             __syncthreads();
;             MS_XSLOAD(0); MS_WLOAD(0, 0); MS_WLOAD(1, 1);
;             MS_WCOMMIT(0, 0); MS_WLOAD(0, 2);
;             MS_XSWRITE(0); MS_XSLOAD(1);
;             __syncthreads();
; #pragma unroll 1
;             for (int t = 0; t < NT; t += 2) { MS_STEP(0, 1, t); MS_STEP(1, 0, t + 1); }
	v_mfma_f32_16x16x32_bf16 v[124:127], v[210:213], v[164:167], v[124:127]
	v_mfma_f32_16x16x32_bf16 v[66:69], v[210:213], v[190:193], v[66:69]
	v_add_u32_e32 v216, v173, v175
	ds_read_b128 v[164:167], v216 offset:32768
	ds_read_b128 v[190:193], v216 offset:34816
	v_add_u32_e32 v217, v176, v175
	ds_read_b128 v[198:201], v217
	ds_read_b128 v[202:205], v217 offset:2048
	ds_read_b128 v[206:209], v217 offset:4096
	ds_read_b128 v[210:213], v217 offset:6144
	s_waitcnt lgkmcnt(3)
	v_mfma_f32_16x16x32_bf16 v[152:155], v[198:201], v[164:167], v[152:155]
	v_mfma_f32_16x16x32_bf16 v[120:123], v[198:201], v[190:193], v[120:123]
	s_waitcnt lgkmcnt(2)
	v_mfma_f32_16x16x32_bf16 v[148:151], v[202:205], v[164:167], v[148:151]
	v_mfma_f32_16x16x32_bf16 v[96:99], v[202:205], v[190:193], v[96:99]
	s_waitcnt lgkmcnt(1)
	v_mfma_f32_16x16x32_bf16 v[144:147], v[206:209], v[164:167], v[144:147]
	v_mfma_f32_16x16x32_bf16 v[86:89], v[206:209], v[190:193], v[86:89]
	s_waitcnt lgkmcnt(0)
	v_mfma_f32_16x16x32_bf16 v[140:143], v[210:213], v[164:167], v[140:143]
	v_mfma_f32_16x16x32_bf16 v[82:85], v[210:213], v[190:193], v[82:85]
	ds_read_b128 v[198:201], v217 offset:8192
	ds_read_b128 v[202:205], v217 offset:10240
	ds_read_b128 v[206:209], v217 offset:12288
	ds_read_b128 v[210:213], v217 offset:14336
	s_min_u32 s33, s2, 5
	s_lshl_b32 s33, s33, 7
	s_waitcnt vmcnt(7)
	ds_write_b128 v189, v[104:107] offset:38912
	s_waitcnt vmcnt(6)
	ds_write_b128 v181, v[92:95] offset:39936
	s_waitcnt vmcnt(5)
	ds_write_b128 v189, v[112:115] offset:40960
	s_waitcnt vmcnt(4)
	ds_write_b128 v181, v[116:119] offset:41984
	s_addk_i32 s33, 0x100
	s_cmp_lt_u32 s2, 6
	s_cbranch_scc1 .Lxl_nx1
	s_cmp_eq_u32 s84, 0
	s_cbranch_scc1 .Lxl_nx1
	s_mov_b32 s33, 0
	v_add_u32_e32 v240, s87, v162
	v_min_i32_e32 v241, s86, v240
	v_add_u32_e32 v241, s88, v241
	v_lshl_or_b32 v182, v241, 10, v163
	v_or_b32_e32 v241, 8, v240
	v_min_i32_e32 v241, s86, v241
	v_add_u32_e32 v241, s88, v241
	v_lshl_or_b32 v183, v241, 10, v163
	v_add_u32_e32 v241, 0x80, v240
	v_min_i32_e32 v241, s86, v241
	v_add_u32_e32 v241, s88, v241
	v_lshl_or_b32 v184, v241, 10, v163
	v_add_u32_e32 v241, 0x88, v240
	v_min_i32_e32 v241, s86, v241
	v_add_u32_e32 v241, s88, v241
	v_lshl_or_b32 v185, v241, 10, v163
	v_add_u32_e32 v241, 0x100, v240
	v_min_i32_e32 v241, s86, v241
	v_add_u32_e32 v241, s88, v241
	v_lshl_or_b32 v186, v241, 10, v163
	v_add_u32_e32 v241, 0x108, v240
	v_min_i32_e32 v241, s86, v241
	v_add_u32_e32 v241, s88, v241
	v_lshl_or_b32 v187, v241, 10, v163
.Lxl_nx1:
	s_waitcnt lgkmcnt(7)
	v_mfma_f32_16x16x32_bf16 v[136:139], v[198:201], v[164:167], v[136:139]
	buffer_load_dwordx4 v[92:95], v182, s[4:7], s33 offen
	buffer_load_dwordx4 v[100:103], v183, s[4:7], s33 offen
	buffer_load_dwordx4 v[104:107], v184, s[4:7], s33 offen
	buffer_load_dwordx4 v[108:111], v185, s[4:7], s33 offen
	s_min_u32 s33, s2, 3
	s_waitcnt lgkmcnt(0)
	v_mfma_f32_16x16x32_bf16 v[132:135], v[202:205], v[164:167], v[132:135]
	s_barrier
	s_lshl_b32 s33, s33, 19
	v_mfma_f32_16x16x32_bf16 v[128:131], v[206:209], v[164:167], v[128:131]
	s_bitset1_b32 s33, 21
	s_sub_i32 s40, s2, 4
	s_lshl_b32 s40, s40, 19
	s_add_i32 s40, s40, s85
	s_cmp_gt_u32 s2, 3
	s_cselect_b32 s33, s40, s33
	v_mfma_f32_16x16x32_bf16 v[124:127], v[210:213], v[164:167], v[124:127]
	v_cvt_pk_bf16_f32 v164, v18, v22
	v_cvt_pk_bf16_f32 v165, v26, v30
	v_cvt_pk_bf16_f32 v18, v19, v23
	v_cvt_pk_bf16_f32 v19, v27, v31
	ds_write2_b64 v188, v[164:165], v[18:19] offset1:16
	v_cvt_pk_bf16_f32 v18, v20, v24
	v_cvt_pk_bf16_f32 v19, v28, v32
	v_cvt_pk_bf16_f32 v20, v21, v25
	v_cvt_pk_bf16_f32 v21, v29, v33
	ds_write2_b64 v180, v[18:19], v[20:21] offset0:32 offset1:48
	buffer_load_dwordx4 v[18:21], v160, s[8:11], s33 offen nt
	buffer_load_dwordx4 v[22:25], v90, s[8:11], s33 offen nt
	buffer_load_dwordx4 v[26:29], v178, s[8:11], s33 offen nt
	buffer_load_dwordx4 v[30:33], v179, s[8:11], s33 offen nt
	v_mfma_f32_16x16x32_bf16 v[78:81], v[198:201], v[190:193], v[78:81]
	v_mfma_f32_16x16x32_bf16 v[74:77], v[202:205], v[190:193], v[74:77]
	v_mfma_f32_16x16x32_bf16 v[70:73], v[206:209], v[190:193], v[70:73]
	v_mfma_f32_16x16x32_bf16 v[66:69], v[210:213], v[190:193], v[66:69]
	ds_read_b128 v[164:167], v214 offset:38912
	ds_read_b128 v[190:193], v214 offset:40960
	ds_read_b128 v[198:201], v215 offset:16384
	ds_read_b128 v[202:205], v215 offset:18432
	ds_read_b128 v[206:209], v215 offset:20480
	ds_read_b128 v[210:213], v215 offset:22528
	s_waitcnt lgkmcnt(3)
	v_mfma_f32_16x16x32_bf16 v[152:155], v[198:201], v[164:167], v[152:155]
	v_mfma_f32_16x16x32_bf16 v[120:123], v[198:201], v[190:193], v[120:123]
	s_waitcnt lgkmcnt(2)
	v_mfma_f32_16x16x32_bf16 v[148:151], v[202:205], v[164:167], v[148:151]
	v_mfma_f32_16x16x32_bf16 v[96:99], v[202:205], v[190:193], v[96:99]
	s_waitcnt lgkmcnt(1)
	v_mfma_f32_16x16x32_bf16 v[144:147], v[206:209], v[164:167], v[144:147]
	v_mfma_f32_16x16x32_bf16 v[86:89], v[206:209], v[190:193], v[86:89]
	s_waitcnt lgkmcnt(0)
	v_mfma_f32_16x16x32_bf16 v[140:143], v[210:213], v[164:167], v[140:143]
	v_mfma_f32_16x16x32_bf16 v[82:85], v[210:213], v[190:193], v[82:85]
	ds_read_b128 v[198:201], v215 offset:24576
	ds_read_b128 v[202:205], v215 offset:26624
	ds_read_b128 v[206:209], v215 offset:28672
	ds_read_b128 v[210:213], v215 offset:30720
	s_waitcnt lgkmcnt(3)
	v_mfma_f32_16x16x32_bf16 v[136:139], v[198:201], v[164:167], v[136:139]
	v_mfma_f32_16x16x32_bf16 v[78:81], v[198:201], v[190:193], v[78:81]
	s_waitcnt lgkmcnt(2)
	v_mfma_f32_16x16x32_bf16 v[132:135], v[202:205], v[164:167], v[132:135]
	v_mfma_f32_16x16x32_bf16 v[74:77], v[202:205], v[190:193], v[74:77]
	s_waitcnt lgkmcnt(1)
; DI unsigned pk2(float a, float b) { f32x2 v = {a, b}; bf16x2_t r = __builtin_convertvector(v, bf16x2_t); return __builtin_bit_cast(unsigned, r); }
; DI float sigmoidf_(float x) { return 1.f / (1.f + __expf(-x)); }
;     ...
; #pragma unroll
;             for (int mt = 0; mt < 3; ++mt) { const int tok = rp + wave * 48 + mt * 16 + tk;
;                 if (tok < M) {
;                     if (MODE == 0) { bf16* o = (bf16*)(ws + o_hid) + (size_t)(row0 + tok) * DEXP + slab * 64 + 4 * q;
; #pragma unroll
;                         for (int j = 0; j < 4; ++j) { float h[4];
; #pragma unroll
;                             for (int i = 0; i < 4; ++i) { const float gt = acc[mt][j][i]; h[i] = gt * sigmoidf_(gt) * acc[mt][j + 4][i]; }
;                             *(u32x2*)(o + 16 * j) = (u32x2){pk2(h[0], h[1]), pk2(h[2], h[3])}; }
;                     } else { bf16* o = (bf16*)(ws + o_yr) + (size_t)(row0 + tok) * D + slab * 128 + 4 * q;
; #pragma unroll
;                         for (int j = 0; j < 8; ++j) *(u32x2*)(o + 16 * j) = (u32x2){pk2(acc[mt][j][0], acc[mt][j][1]), pk2(acc[mt][j][2], acc[mt][j][3])}; } } }
	v_mfma_f32_16x16x32_bf16 v[128:131], v[206:209], v[164:167], v[128:131]
	v_mfma_f32_16x16x32_bf16 v[70:73], v[206:209], v[190:193], v[70:73]
	s_waitcnt lgkmcnt(0)
	v_mfma_f32_16x16x32_bf16 v[124:127], v[210:213], v[164:167], v[124:127]
	v_mfma_f32_16x16x32_bf16 v[66:69], v[210:213], v[190:193], v[66:69]
	ds_read_b128 v[164:167], v216 offset:38912
	ds_read_b128 v[190:193], v216 offset:40960
	ds_read_b128 v[198:201], v217 offset:16384
	ds_read_b128 v[202:205], v217 offset:18432
	ds_read_b128 v[206:209], v217 offset:20480
	ds_read_b128 v[210:213], v217 offset:22528
	s_waitcnt lgkmcnt(3)
	v_mfma_f32_16x16x32_bf16 v[152:155], v[198:201], v[164:167], v[152:155]
	v_mfma_f32_16x16x32_bf16 v[120:123], v[198:201], v[190:193], v[120:123]
	s_waitcnt lgkmcnt(2)
	v_mfma_f32_16x16x32_bf16 v[148:151], v[202:205], v[164:167], v[148:151]
	v_mfma_f32_16x16x32_bf16 v[96:99], v[202:205], v[190:193], v[96:99]
	s_waitcnt lgkmcnt(1)
	v_mfma_f32_16x16x32_bf16 v[144:147], v[206:209], v[164:167], v[144:147]
	v_mfma_f32_16x16x32_bf16 v[86:89], v[206:209], v[190:193], v[86:89]
	s_waitcnt lgkmcnt(0)
	v_mfma_f32_16x16x32_bf16 v[140:143], v[210:213], v[164:167], v[140:143]
	v_mfma_f32_16x16x32_bf16 v[82:85], v[210:213], v[190:193], v[82:85]
	ds_read_b128 v[198:201], v217 offset:24576
	ds_read_b128 v[202:205], v217 offset:26624
	ds_read_b128 v[206:209], v217 offset:28672
	ds_read_b128 v[210:213], v217 offset:30720
	s_lshl_b32 s3, s3, 7
	s_waitcnt vmcnt(7)
	ds_write_b128 v189, v[92:95] offset:32768
	s_waitcnt vmcnt(6)
	ds_write_b128 v181, v[100:103] offset:33792
	s_waitcnt vmcnt(5)
	ds_write_b128 v189, v[104:107] offset:34816
	s_waitcnt vmcnt(4)
	ds_write_b128 v181, v[108:111] offset:35840
	s_addk_i32 s3, 0x180
	s_cmp_eq_u32 s2, 6
	s_cselect_b32 s40, s84, 0
	s_cmp_lg_u32 s40, 0
	s_cselect_b32 s3, 0x80, s3
	buffer_load_dwordx4 v[104:107], v182, s[4:7], s3 offen
	buffer_load_dwordx4 v[92:95], v183, s[4:7], s3 offen
	buffer_load_dwordx4 v[112:115], v184, s[4:7], s3 offen
	buffer_load_dwordx4 v[116:119], v185, s[4:7], s3 offen
	s_waitcnt lgkmcnt(7)
	v_mfma_f32_16x16x32_bf16 v[136:139], v[198:201], v[164:167], v[136:139]
	s_cmp_gt_u32 s2, 5
	s_waitcnt lgkmcnt(0)
	s_barrier
	v_mfma_f32_16x16x32_bf16 v[78:81], v[198:201], v[190:193], v[78:81]
	v_mfma_f32_16x16x32_bf16 v[132:135], v[202:205], v[164:167], v[132:135]
	v_mfma_f32_16x16x32_bf16 v[74:77], v[202:205], v[190:193], v[74:77]
	v_mfma_f32_16x16x32_bf16 v[128:131], v[206:209], v[164:167], v[128:131]
	v_mfma_f32_16x16x32_bf16 v[70:73], v[206:209], v[190:193], v[70:73]
	v_mfma_f32_16x16x32_bf16 v[124:127], v[210:213], v[164:167], v[124:127]
	v_mfma_f32_16x16x32_bf16 v[66:69], v[210:213], v[190:193], v[66:69]
	s_cbranch_scc0 .Lmoe_l_b
.Lmoe_l_done:
	v_add_u32_e32 v240, s31, v177
	v_cmp_gt_i32_e32 vcc, s30, v240
	s_and_saveexec_b64 s[2:3], vcc
	s_cbranch_execz .LBB0_1788
	v_add_u32_e32 v242, s24, v240
	v_ashrrev_i32_e32 v243, 31, v242
	v_lshlrev_b64 v[242:243], 12, v[242:243]
	v_lshl_add_u64 v[242:243], v[158:159], 0, v[242:243]
	v_cvt_pk_bf16_f32 v244, v152, v153
	v_cvt_pk_bf16_f32 v245, v154, v155
	global_store_dwordx2 v[242:243], v[244:245], off
	v_cvt_pk_bf16_f32 v244, v148, v149
	v_cvt_pk_bf16_f32 v245, v150, v151
	global_store_dwordx2 v[242:243], v[244:245], off offset:32
	v_cvt_pk_bf16_f32 v244, v144, v145
	v_cvt_pk_bf16_f32 v245, v146, v147
	global_store_dwordx2 v[242:243], v[244:245], off offset:64
	v_cvt_pk_bf16_f32 v244, v140, v141
	v_cvt_pk_bf16_f32 v245, v142, v143
	global_store_dwordx2 v[242:243], v[244:245], off offset:96
	v_cvt_pk_bf16_f32 v244, v136, v137
	v_cvt_pk_bf16_f32 v245, v138, v139
	global_store_dwordx2 v[242:243], v[244:245], off offset:128
	v_cvt_pk_bf16_f32 v244, v132, v133
	v_cvt_pk_bf16_f32 v245, v134, v135
	global_store_dwordx2 v[242:243], v[244:245], off offset:160
	v_cvt_pk_bf16_f32 v244, v128, v129
	v_cvt_pk_bf16_f32 v245, v130, v131
	global_store_dwordx2 v[242:243], v[244:245], off offset:192
	v_cvt_pk_bf16_f32 v244, v124, v125
	v_cvt_pk_bf16_f32 v245, v126, v127
	global_store_dwordx2 v[242:243], v[244:245], off offset:224
; DI unsigned pk2(float a, float b) { f32x2 v = {a, b}; bf16x2_t r = __builtin_convertvector(v, bf16x2_t); return __builtin_bit_cast(unsigned, r); }
; DI float sigmoidf_(float x) { return 1.f / (1.f + __expf(-x)); }
;     ...
;             f32x4 acc[3][8];
; #pragma unroll
;             for (int mt = 0; mt < 3; ++mt)
; #pragma unroll
;                 for (int j = 0; j < 8; ++j) acc[mt][j] = (f32x4){0.f, 0.f, 0.f, 0.f};
;     ...
; #pragma unroll
;             for (int mt = 0; mt < 3; ++mt) { const int tok = rp + wave * 48 + mt * 16 + tk;
;                 if (tok < M) {
;                     if (MODE == 0) { bf16* o = (bf16*)(ws + o_hid) + (size_t)(row0 + tok) * DEXP + slab * 64 + 4 * q;
; #pragma unroll
;                         for (int j = 0; j < 4; ++j) { float h[4];
; #pragma unroll
;                             for (int i = 0; i < 4; ++i) { const float gt = acc[mt][j][i]; h[i] = gt * sigmoidf_(gt) * acc[mt][j + 4][i]; }
;                             *(u32x2*)(o + 16 * j) = (u32x2){pk2(h[0], h[1]), pk2(h[2], h[3])}; }
;                     } else { bf16* o = (bf16*)(ws + o_yr) + (size_t)(row0 + tok) * D + slab * 128 + 4 * q;
; #pragma unroll
;                         for (int j = 0; j < 8; ++j) *(u32x2*)(o + 16 * j) = (u32x2){pk2(acc[mt][j][0], acc[mt][j][1]), pk2(acc[mt][j][2], acc[mt][j][3])}; } } }
.LBB0_1788:
	s_or_b64 exec, exec, s[2:3]
	v_add_u32_e32 v241, 0x80, v240
	v_cmp_gt_i32_e32 vcc, s30, v241
	s_and_saveexec_b64 s[2:3], vcc
	s_cbranch_execz .LBB0_1790
	v_add_u32_e32 v242, s24, v241
	v_ashrrev_i32_e32 v243, 31, v242
	v_lshlrev_b64 v[242:243], 12, v[242:243]
	v_lshl_add_u64 v[242:243], v[158:159], 0, v[242:243]
	v_cvt_pk_bf16_f32 v244, v120, v121
	v_cvt_pk_bf16_f32 v245, v122, v123
	global_store_dwordx2 v[242:243], v[244:245], off
	v_cvt_pk_bf16_f32 v244, v96, v97
	v_cvt_pk_bf16_f32 v245, v98, v99
	global_store_dwordx2 v[242:243], v[244:245], off offset:32
	v_cvt_pk_bf16_f32 v244, v86, v87
	v_cvt_pk_bf16_f32 v245, v88, v89
	global_store_dwordx2 v[242:243], v[244:245], off offset:64
	v_cvt_pk_bf16_f32 v244, v82, v83
	v_cvt_pk_bf16_f32 v245, v84, v85
	global_store_dwordx2 v[242:243], v[244:245], off offset:96
	v_cvt_pk_bf16_f32 v244, v78, v79
	v_cvt_pk_bf16_f32 v245, v80, v81
	global_store_dwordx2 v[242:243], v[244:245], off offset:128
	v_cvt_pk_bf16_f32 v244, v74, v75
	v_cvt_pk_bf16_f32 v245, v76, v77
	global_store_dwordx2 v[242:243], v[244:245], off offset:160
	v_cvt_pk_bf16_f32 v244, v70, v71
	v_cvt_pk_bf16_f32 v245, v72, v73
	global_store_dwordx2 v[242:243], v[244:245], off offset:192
	v_cvt_pk_bf16_f32 v244, v66, v67
	v_cvt_pk_bf16_f32 v245, v68, v69
	global_store_dwordx2 v[242:243], v[244:245], off offset:224
.LBB0_1790:
	s_or_b64 exec, exec, s[2:3]
	v_add_u32_e32 v240, 0x100, v240
	v_cmp_gt_i32_e32 vcc, s30, v240
	s_and_saveexec_b64 s[2:3], vcc
	s_cbranch_execz .LBB0_1783
	v_add_u32_e32 v240, s24, v240
	v_ashrrev_i32_e32 v241, 31, v240
	v_lshlrev_b64 v[240:241], 12, v[240:241]
	v_lshl_add_u64 v[240:241], v[158:159], 0, v[240:241]
	v_cvt_pk_bf16_f32 v242, v62, v63
	v_cvt_pk_bf16_f32 v243, v64, v65
	global_store_dwordx2 v[240:241], v[242:243], off
	v_cvt_pk_bf16_f32 v242, v58, v59
	v_cvt_pk_bf16_f32 v243, v60, v61
	global_store_dwordx2 v[240:241], v[242:243], off offset:32
	v_cvt_pk_bf16_f32 v242, v54, v55
	v_cvt_pk_bf16_f32 v243, v56, v57
	global_store_dwordx2 v[240:241], v[242:243], off offset:64
	v_cvt_pk_bf16_f32 v242, v50, v51
	v_cvt_pk_bf16_f32 v243, v52, v53
	global_store_dwordx2 v[240:241], v[242:243], off offset:96
	v_cvt_pk_bf16_f32 v242, v46, v47
	v_cvt_pk_bf16_f32 v243, v48, v49
	global_store_dwordx2 v[240:241], v[242:243], off offset:128
	v_cvt_pk_bf16_f32 v242, v42, v43
	v_cvt_pk_bf16_f32 v243, v44, v45
	global_store_dwordx2 v[240:241], v[242:243], off offset:160
	v_cvt_pk_bf16_f32 v242, v38, v39
	v_cvt_pk_bf16_f32 v243, v40, v41
	global_store_dwordx2 v[240:241], v[242:243], off offset:192
	v_cvt_pk_bf16_f32 v242, v34, v35
	v_cvt_pk_bf16_f32 v243, v36, v37
	global_store_dwordx2 v[240:241], v[242:243], off offset:224
	s_branch .LBB0_1783
.Lxl_fast:
	s_mov_b32 s2, -2
	v_mov_b32_e32 v34, 0
	v_mov_b32_e32 v35, 0
	v_mov_b32_e32 v36, 0
	v_mov_b32_e32 v37, 0
	v_mov_b32_e32 v38, 0
	v_mov_b32_e32 v39, 0
	v_mov_b32_e32 v40, 0
	v_mov_b32_e32 v41, 0
	v_mov_b32_e32 v42, 0
	v_mov_b32_e32 v43, 0
	v_mov_b32_e32 v44, 0
	v_mov_b32_e32 v45, 0
	v_mov_b32_e32 v46, 0
	v_mov_b32_e32 v47, 0
	v_mov_b32_e32 v48, 0
	v_mov_b32_e32 v49, 0
	v_mov_b32_e32 v50, 0
	v_mov_b32_e32 v51, 0
	v_mov_b32_e32 v52, 0
	v_mov_b32_e32 v53, 0
	v_mov_b32_e32 v54, 0
	v_mov_b32_e32 v55, 0
	v_mov_b32_e32 v56, 0
	v_mov_b32_e32 v57, 0
	v_mov_b32_e32 v58, 0
	v_mov_b32_e32 v59, 0
	v_mov_b32_e32 v60, 0
	v_mov_b32_e32 v61, 0
	v_mov_b32_e32 v62, 0
	v_mov_b32_e32 v63, 0
	v_mov_b32_e32 v64, 0
	v_mov_b32_e32 v65, 0
	v_mov_b32_e32 v66, 0
	v_mov_b32_e32 v67, 0
	v_mov_b32_e32 v68, 0
	v_mov_b32_e32 v69, 0
	v_mov_b32_e32 v70, 0
	v_mov_b32_e32 v71, 0
	v_mov_b32_e32 v72, 0
	v_mov_b32_e32 v73, 0
	v_mov_b32_e32 v74, 0
	v_mov_b32_e32 v75, 0
	v_mov_b32_e32 v76, 0
	v_mov_b32_e32 v77, 0
	v_mov_b32_e32 v78, 0
	v_mov_b32_e32 v79, 0
	v_mov_b32_e32 v80, 0
	v_mov_b32_e32 v81, 0
	v_mov_b32_e32 v82, 0
	v_mov_b32_e32 v83, 0
	v_mov_b32_e32 v84, 0
	v_mov_b32_e32 v85, 0
	v_mov_b32_e32 v86, 0
	v_mov_b32_e32 v87, 0
	v_mov_b32_e32 v88, 0
	v_mov_b32_e32 v89, 0
	v_mov_b32_e32 v96, 0
	v_mov_b32_e32 v97, 0
	v_mov_b32_e32 v98, 0
	v_mov_b32_e32 v99, 0
	v_mov_b32_e32 v120, 0
	v_mov_b32_e32 v121, 0
	v_mov_b32_e32 v122, 0
	v_mov_b32_e32 v123, 0
	v_mov_b32_e32 v124, 0
	v_mov_b32_e32 v125, 0
	v_mov_b32_e32 v126, 0
	v_mov_b32_e32 v127, 0
	v_mov_b32_e32 v128, 0
	v_mov_b32_e32 v129, 0
	v_mov_b32_e32 v130, 0
	v_mov_b32_e32 v131, 0
	v_mov_b32_e32 v132, 0
	v_mov_b32_e32 v133, 0
	v_mov_b32_e32 v134, 0
	v_mov_b32_e32 v135, 0
	v_mov_b32_e32 v136, 0
	v_mov_b32_e32 v137, 0
	v_mov_b32_e32 v138, 0
	v_mov_b32_e32 v139, 0
	v_mov_b32_e32 v140, 0
	v_mov_b32_e32 v141, 0
	v_mov_b32_e32 v142, 0
	v_mov_b32_e32 v143, 0
	v_mov_b32_e32 v144, 0
	v_mov_b32_e32 v145, 0
	v_mov_b32_e32 v146, 0
	v_mov_b32_e32 v147, 0
	v_mov_b32_e32 v148, 0
	v_mov_b32_e32 v149, 0
	v_mov_b32_e32 v150, 0
	v_mov_b32_e32 v151, 0
	v_mov_b32_e32 v152, 0
	v_mov_b32_e32 v153, 0
	v_mov_b32_e32 v154, 0
	v_mov_b32_e32 v155, 0
	s_branch .Lxl_disp
.LBB0_1792:
	s_mov_b32 s10, 0x400000
	v_readlane_b32 s0, v255, 32
	s_add_i32 s0, s0, 11
	s_cmp_ge_i32 s0, s77
	s_cbranch_scc0 .LBB0_1793
	s_getpc_b64 s[98:99]
